# v21 + barrier leaders no longer bump the (now unused) per-XCD generation word
# baseline (speedup 1.0000x reference)
.LBB0_123:
	s_or_b64 exec, exec, s[6:7]
	s_mov_b64 s[6:7], exec
	v_mbcnt_lo_u32_b32 v1, s6, 0
	v_mbcnt_hi_u32_b32 v1, s7, v1
	v_cmp_eq_u32_e32 vcc, 0, v1
	s_waitcnt vmcnt(0)
	buffer_inv sc1
	s_and_saveexec_b64 s[8:9], vcc
	s_cbranch_execz .LBB0_125
	s_bcnt1_i32_b64 s6, s[6:7]
	v_mov_b32_e32 v1, 0x2000
	v_mov_b32_e32 v2, s6
.LBB0_125:
	s_or_b64 exec, exec, s[8:9]
	s_waitcnt vmcnt(0)

.LBB0_186:
	s_or_b64 exec, exec, s[6:7]
	s_mov_b64 s[6:7], exec
	v_mbcnt_lo_u32_b32 v1, s6, 0
	v_mbcnt_hi_u32_b32 v1, s7, v1
	v_cmp_eq_u32_e32 vcc, 0, v1
	s_waitcnt vmcnt(0)
	buffer_inv sc1
	s_and_saveexec_b64 s[8:9], vcc
	s_cbranch_execz .LBB0_188
	s_bcnt1_i32_b64 s6, s[6:7]
	v_mov_b32_e32 v1, 0x2000
	v_mov_b32_e32 v2, s6
.LBB0_188:
	s_or_b64 exec, exec, s[8:9]
	s_waitcnt vmcnt(0)

.LBB0_673:
	s_or_b64 exec, exec, s[6:7]
	s_mov_b64 s[6:7], exec
	v_mbcnt_lo_u32_b32 v1, s6, 0
	v_mbcnt_hi_u32_b32 v1, s7, v1
	v_cmp_eq_u32_e32 vcc, 0, v1
	s_waitcnt vmcnt(0)
	buffer_inv sc1
	s_and_saveexec_b64 s[8:9], vcc
	s_cbranch_execz .LBB0_675
	s_bcnt1_i32_b64 s6, s[6:7]
	v_mov_b32_e32 v1, 0x2000
	v_mov_b32_e32 v2, s6
.LBB0_675:
	s_or_b64 exec, exec, s[8:9]
	s_waitcnt vmcnt(0)

.LBB0_863:
	s_or_b64 exec, exec, s[6:7]
	s_mov_b64 s[6:7], exec
	v_mbcnt_lo_u32_b32 v1, s6, 0
	v_mbcnt_hi_u32_b32 v1, s7, v1
	v_cmp_eq_u32_e32 vcc, 0, v1
	s_waitcnt vmcnt(0)
	buffer_inv sc1
	s_and_saveexec_b64 s[8:9], vcc
	s_cbranch_execz .LBB0_865
	s_bcnt1_i32_b64 s6, s[6:7]
	v_mov_b32_e32 v1, 0x2000
	v_mov_b32_e32 v2, s6
.LBB0_865:
	s_or_b64 exec, exec, s[8:9]
	s_waitcnt vmcnt(0)

.LBB0_928:
	s_or_b64 exec, exec, s[6:7]
	s_mov_b64 s[6:7], exec
	v_mbcnt_lo_u32_b32 v1, s6, 0
	v_mbcnt_hi_u32_b32 v1, s7, v1
	v_cmp_eq_u32_e32 vcc, 0, v1
	s_waitcnt vmcnt(0)
	buffer_inv sc1
	s_and_saveexec_b64 s[8:9], vcc
	s_cbranch_execz .LBB0_930
	s_bcnt1_i32_b64 s6, s[6:7]
	v_mov_b32_e32 v1, 0x2000
	v_mov_b32_e32 v2, s6
.LBB0_930:
	s_or_b64 exec, exec, s[8:9]
	s_waitcnt vmcnt(0)

.LBB0_1036:
	s_or_b64 exec, exec, s[6:7]
	s_mov_b64 s[6:7], exec
	v_mbcnt_lo_u32_b32 v1, s6, 0
	v_mbcnt_hi_u32_b32 v1, s7, v1
	v_cmp_eq_u32_e32 vcc, 0, v1
	s_waitcnt vmcnt(0)
	buffer_inv sc1
	s_and_saveexec_b64 s[8:9], vcc
	s_cbranch_execz .LBB0_1038
	s_bcnt1_i32_b64 s6, s[6:7]
	v_mov_b32_e32 v1, 0x2000
	v_mov_b32_e32 v2, s6
.LBB0_1038:
	s_or_b64 exec, exec, s[8:9]
	s_waitcnt vmcnt(0)

.LBB0_1120:
	s_or_b64 exec, exec, s[6:7]
	s_mov_b64 s[6:7], exec
	v_mbcnt_lo_u32_b32 v1, s6, 0
	v_mbcnt_hi_u32_b32 v1, s7, v1
	v_cmp_eq_u32_e32 vcc, 0, v1
	s_waitcnt vmcnt(0)
	buffer_inv sc1
	s_and_saveexec_b64 s[8:9], vcc
	s_cbranch_execz .LBB0_1122
	s_bcnt1_i32_b64 s6, s[6:7]
	v_mov_b32_e32 v1, 0x2000
	v_mov_b32_e32 v2, s6
.LBB0_1122:
	s_or_b64 exec, exec, s[8:9]
	s_waitcnt vmcnt(0)

.LBB0_1204:
	s_or_b64 exec, exec, s[6:7]
	s_mov_b64 s[6:7], exec
	v_mbcnt_lo_u32_b32 v1, s6, 0
	v_mbcnt_hi_u32_b32 v1, s7, v1
	v_cmp_eq_u32_e32 vcc, 0, v1
	s_waitcnt vmcnt(0)
	buffer_inv sc1
	s_and_saveexec_b64 s[8:9], vcc
	s_cbranch_execz .LBB0_1206
	s_bcnt1_i32_b64 s6, s[6:7]
	v_mov_b32_e32 v1, 0x2000
	v_mov_b32_e32 v2, s6
.LBB0_1206:
	s_or_b64 exec, exec, s[8:9]
	s_waitcnt vmcnt(0)

.LBB0_1508:
	s_or_b64 exec, exec, s[6:7]
	s_mov_b64 s[6:7], exec
	v_mbcnt_lo_u32_b32 v1, s6, 0
	v_mbcnt_hi_u32_b32 v1, s7, v1
	v_cmp_eq_u32_e32 vcc, 0, v1
	s_waitcnt vmcnt(0)
	buffer_inv sc1
	s_and_saveexec_b64 s[8:9], vcc
	s_cbranch_execz .LBB0_1510
	s_bcnt1_i32_b64 s6, s[6:7]
	v_mov_b32_e32 v1, 0x2000
	v_mov_b32_e32 v2, s6
.LBB0_1510:
	s_or_b64 exec, exec, s[8:9]
	s_waitcnt vmcnt(0)

.LBB0_1588:
	s_or_b64 exec, exec, s[6:7]
	s_mov_b64 s[6:7], exec
	v_mbcnt_lo_u32_b32 v1, s6, 0
	v_mbcnt_hi_u32_b32 v1, s7, v1
	v_cmp_eq_u32_e32 vcc, 0, v1
	s_waitcnt vmcnt(0)
	buffer_inv sc1
	s_and_saveexec_b64 s[8:9], vcc
	s_cbranch_execz .LBB0_1590
	s_bcnt1_i32_b64 s6, s[6:7]
	v_mov_b32_e32 v1, 0x2000
	v_mov_b32_e32 v2, s6
.LBB0_1590:
	s_or_b64 exec, exec, s[8:9]
	s_waitcnt vmcnt(0)

.LBB0_1908:
	s_or_b64 exec, exec, s[6:7]
	s_mov_b64 s[6:7], exec
	v_mbcnt_lo_u32_b32 v1, s6, 0
	v_mbcnt_hi_u32_b32 v1, s7, v1
	v_cmp_eq_u32_e32 vcc, 0, v1
	s_waitcnt vmcnt(0)
	buffer_inv sc1
	s_and_saveexec_b64 s[8:9], vcc
	s_cbranch_execz .LBB0_1910
	s_bcnt1_i32_b64 s6, s[6:7]
	v_mov_b32_e32 v1, 0x2000
	v_mov_b32_e32 v2, s6
.LBB0_1910:
	s_or_b64 exec, exec, s[8:9]
	s_waitcnt vmcnt(0)

.LBB0_2056:
	s_or_b64 exec, exec, s[6:7]
	s_mov_b64 s[6:7], exec
	v_mbcnt_lo_u32_b32 v0, s6, 0
	v_mbcnt_hi_u32_b32 v0, s7, v0
	v_cmp_eq_u32_e32 vcc, 0, v0
	s_waitcnt vmcnt(0)
	buffer_inv sc1
	s_and_saveexec_b64 s[8:9], vcc
	s_cbranch_execz .LBB0_2058
	s_bcnt1_i32_b64 s6, s[6:7]
	v_mov_b32_e32 v0, 0x2000
	v_mov_b32_e32 v1, s6
.LBB0_2058:
	s_or_b64 exec, exec, s[8:9]
	s_waitcnt vmcnt(0)
